# v6: NSA tile loops - LDS-DMA issue for tile t+2 moved onto the high-priority waves 0-3 (each also issues its twin wave's four pieces), waves 4-7 skip it
# baseline (speedup 1.0000x reference)
.LBB0_726:
	s_andn2_b64 vcc, exec, s[8:9]
	s_cbranch_vccnz .LBB0_728
	v_readfirstlane_b32 s99, v0
	s_bitcmp1_b32 s99, 8
	s_cbranch_scc0 .Lnsa_w0
	s_waitcnt vmcnt(0)
.Lnsa_w0:
	s_waitcnt vmcnt(4)
.LBB0_728:
	s_add_i32 s8, s10, 2
	s_cmp_lt_u32 s8, s95
	s_mov_b64 s[8:9], -1
	s_barrier
	s_cbranch_scc1 .LBB0_730
	s_lshl_b32 s11, s92, 15
	s_mov_b64 s[8:9], 0
.LBB0_730:
	s_andn2_b64 vcc, exec, s[8:9]
	s_cbranch_vccnz .LBB0_732
	v_readfirstlane_b32 s99, v0
	s_bitcmp1_b32 s99, 8
	s_cbranch_scc0 .Lnsa_d0
	s_lshl_b32 s11, s92, 15
	s_branch .LBB0_732
.Lnsa_d0:
	s_mov_b32 s100, 0x2000
	s_mov_b32 s101, 0
	v_mov_b32_e32 v4, s22
	ds_read_b32 v6, v4 offset:8
	s_lshl_b32 s11, s92, 15
	s_add_i32 s8, s11, 0xffff8000
	s_cmp_lg_u32 s92, 0
	s_cselect_b32 s8, s8, 0x10000
	s_waitcnt lgkmcnt(0)
	v_add_u32_e32 v7, v6, v189
	v_add_u32_e32 v4, v7, v208
	v_ashrrev_i32_e32 v5, 31, v4
	v_lshlrev_b64 v[4:5], 9, v[4:5]
	s_add_i32 s8, s17, s8
	v_lshl_add_u64 v[4:5], v[132:133], 0, v[4:5]
	s_mov_b32 m0, s8
	s_nop 0
	global_load_lds_dwordx4 v[4:5], off
	s_add_i32 m0, m0, 0x1000
	v_lshl_add_u64 v[4:5], v[4:5], 0, s[100:101]
	global_load_lds_dwordx4 v[4:5], off
	v_add_u32_e32 v4, v6, v188
	v_ashrrev_i32_e32 v5, 31, v4
	v_lshlrev_b64 v[4:5], 9, v[4:5]
	v_lshl_add_u64 v[4:5], v[134:135], 0, v[4:5]
	s_add_i32 m0, s8, 0x4000
	s_nop 0
	global_load_lds_dwordx4 v[4:5], off
	s_add_i32 m0, m0, 0x1000
	v_lshl_add_u64 v[4:5], v[4:5], 0, s[100:101]
	global_load_lds_dwordx4 v[4:5], off
	v_add_u32_e32 v4, v7, v210
	v_ashrrev_i32_e32 v5, 31, v4
	v_lshlrev_b64 v[4:5], 9, v[4:5]
	v_lshl_add_u64 v[4:5], v[132:133], 0, v[4:5]
	s_add_i32 m0, s8, 0x2000
	s_nop 0
	global_load_lds_dwordx4 v[4:5], off
	s_add_i32 m0, m0, 0x1000
	v_lshl_add_u64 v[4:5], v[4:5], 0, s[100:101]
	global_load_lds_dwordx4 v[4:5], off
	v_add_u32_e32 v4, v6, v209
	v_ashrrev_i32_e32 v5, 31, v4
	v_lshlrev_b64 v[4:5], 9, v[4:5]
	v_lshl_add_u64 v[4:5], v[140:141], 0, v[4:5]
	s_add_i32 m0, s8, 0x6000
	s_nop 0
	global_load_lds_dwordx4 v[4:5], off
	s_add_i32 m0, m0, 0x1000
	v_lshl_add_u64 v[4:5], v[4:5], 0, s[100:101]
	global_load_lds_dwordx4 v[4:5], off

.LBB0_742:
	s_andn2_b64 vcc, exec, s[2:3]
	s_cbranch_vccnz .LBB0_744
	v_readfirstlane_b32 s99, v0
	s_bitcmp1_b32 s99, 8
	s_cbranch_scc0 .Lnsa_w1
	s_waitcnt vmcnt(0)
.Lnsa_w1:
	s_waitcnt vmcnt(4)
.LBB0_744:
	s_add_i32 s2, s6, 2
	s_cmp_lt_u32 s2, s95
	s_mov_b64 s[2:3], -1
	s_barrier
	s_cbranch_scc1 .LBB0_746
	s_lshl_b32 s22, s93, 15
	s_mov_b64 s[2:3], 0
.LBB0_746:
	s_andn2_b64 vcc, exec, s[2:3]
	s_cbranch_vccnz .LBB0_748
	v_readfirstlane_b32 s99, v0
	s_bitcmp1_b32 s99, 8
	s_cbranch_scc0 .Lnsa_d1
	s_lshl_b32 s22, s93, 15
	s_branch .LBB0_748
.Lnsa_d1:
	s_mov_b32 s100, 0x2000
	s_mov_b32 s101, 0
	v_mov_b32_e32 v68, s92
	ds_read_b32 v70, v68 offset:8
	s_lshl_b32 s22, s93, 15
	s_add_i32 s2, s22, 0xffff8000
	s_cmp_lg_u32 s93, 0
	s_cselect_b32 s2, s2, 0x10000
	s_waitcnt lgkmcnt(0)
	v_add_u32_e32 v71, v70, v189
	v_add_u32_e32 v68, v71, v208
	v_ashrrev_i32_e32 v69, 31, v68
	v_lshlrev_b64 v[68:69], 9, v[68:69]
	s_add_i32 s2, s17, s2
	v_lshl_add_u64 v[68:69], v[132:133], 0, v[68:69]
	s_mov_b32 m0, s2
	s_nop 0
	global_load_lds_dwordx4 v[68:69], off
	s_add_i32 m0, m0, 0x1000
	v_lshl_add_u64 v[68:69], v[68:69], 0, s[100:101]
	global_load_lds_dwordx4 v[68:69], off
	v_add_u32_e32 v68, v70, v188
	v_ashrrev_i32_e32 v69, 31, v68
	v_lshlrev_b64 v[68:69], 9, v[68:69]
	v_lshl_add_u64 v[68:69], v[134:135], 0, v[68:69]
	s_add_i32 m0, s2, 0x4000
	s_nop 0
	global_load_lds_dwordx4 v[68:69], off
	s_add_i32 m0, m0, 0x1000
	v_lshl_add_u64 v[68:69], v[68:69], 0, s[100:101]
	global_load_lds_dwordx4 v[68:69], off
	v_add_u32_e32 v68, v71, v210
	v_ashrrev_i32_e32 v69, 31, v68
	v_lshlrev_b64 v[68:69], 9, v[68:69]
	v_lshl_add_u64 v[68:69], v[132:133], 0, v[68:69]
	s_add_i32 m0, s2, 0x2000
	s_nop 0
	global_load_lds_dwordx4 v[68:69], off
	s_add_i32 m0, m0, 0x1000
	v_lshl_add_u64 v[68:69], v[68:69], 0, s[100:101]
	global_load_lds_dwordx4 v[68:69], off
	v_add_u32_e32 v68, v70, v209
	v_ashrrev_i32_e32 v69, 31, v68
	v_lshlrev_b64 v[68:69], 9, v[68:69]
	v_lshl_add_u64 v[68:69], v[140:141], 0, v[68:69]
	s_add_i32 m0, s2, 0x6000
	s_nop 0
	global_load_lds_dwordx4 v[68:69], off
	s_add_i32 m0, m0, 0x1000
	v_lshl_add_u64 v[68:69], v[68:69], 0, s[100:101]
	global_load_lds_dwordx4 v[68:69], off

.LBB0_789:
	s_add_i32 s2, s7, 2
	s_cmp_le_i32 s2, s64
	s_mov_b64 s[2:3], -1
	s_barrier
	s_cbranch_scc0 .LBB0_791
	v_readfirstlane_b32 s99, v0
	s_bitcmp1_b32 s99, 8
	s_cbranch_scc0 .Lnsa_d2
	s_lshl_b32 s22, s6, 15
	s_branch .LBB0_793
.Lnsa_d2:
	s_mov_b32 s100, 0x2e000
	s_mov_b32 s101, 0
	v_mov_b32_e32 v2, s17
	ds_read_b32 v2, v2 offset:8
	s_lshl_b32 s22, s6, 15
	s_add_i32 s2, s22, 0xffff8000
	s_cmp_lg_u32 s6, 0
	s_cselect_b32 s10, s2, 0x10000
	s_waitcnt lgkmcnt(0)
	v_add_u32_e32 v70, v2, v189
	v_add_u32_e32 v68, v70, v158
	s_add_i32 s10, s46, s10
	v_mad_i64_i32 v[68:69], s[2:3], v68, s76, v[132:133]
	s_mov_b32 m0, s10
	s_nop 0
	global_load_lds_dwordx4 v[68:69], off
	s_add_i32 m0, m0, 0x1000
	v_lshl_add_u64 v[68:69], v[68:69], 0, s[100:101]
	global_load_lds_dwordx4 v[68:69], off
	v_add_u32_e32 v68, v2, v188
	v_mad_i64_i32 v[68:69], s[2:3], v68, s76, v[134:135]
	s_add_i32 m0, s10, 0x4000
	v_add_u32_e32 v2, v2, v159
	global_load_lds_dwordx4 v[68:69], off
	s_add_i32 m0, m0, 0x1000
	v_lshl_add_u64 v[68:69], v[68:69], 0, s[100:101]
	global_load_lds_dwordx4 v[68:69], off
	v_add_u32_e32 v68, v70, v160
	v_mad_i64_i32 v[68:69], s[2:3], v68, s76, v[132:133]
	s_add_i32 m0, s10, 0x2000
	s_nop 0
	global_load_lds_dwordx4 v[68:69], off
	s_add_i32 m0, m0, 0x1000
	v_lshl_add_u64 v[68:69], v[68:69], 0, s[100:101]
	global_load_lds_dwordx4 v[68:69], off
	v_mad_i64_i32 v[68:69], s[2:3], v2, s76, v[142:143]
	s_add_i32 m0, s10, 0x6000
	s_mov_b64 s[2:3], 0
	global_load_lds_dwordx4 v[68:69], off
	s_add_i32 m0, m0, 0x1000
	v_lshl_add_u64 v[68:69], v[68:69], 0, s[100:101]
	global_load_lds_dwordx4 v[68:69], off

.Lnsa_w3:
	s_waitcnt vmcnt(4)
.LBB0_972:
	s_add_i32 s2, s10, 2
	s_cmp_lt_i32 s2, s17
	s_mov_b64 s[2:3], -1
	s_barrier
	s_cbranch_scc1 .LBB0_974
	s_lshl_b32 s70, s22, 15
	s_mov_b64 s[2:3], 0
.LBB0_974:
	s_andn2_b64 vcc, exec, s[2:3]
	s_cbranch_vccnz .LBB0_976
	v_readfirstlane_b32 s99, v0
	s_bitcmp1_b32 s99, 8
	s_cbranch_scc0 .Lnsa_d3
	s_lshl_b32 s70, s22, 15
	s_branch .LBB0_976
.Lnsa_d3:
	s_mov_b32 s100, 0x2e000
	s_mov_b32 s101, 0
	v_mov_b32_e32 v2, s23
	ds_read_b32 v2, v2 offset:8
	s_lshl_b32 s70, s22, 15
	s_add_i32 s2, s70, 0xffff8000
	s_cmp_lg_u32 s22, 0
	s_cselect_b32 s10, s2, 0x10000
	s_waitcnt lgkmcnt(0)
	v_add_u32_e32 v70, v2, v189
	v_add_u32_e32 v68, v70, v167
	v_mad_i64_i32 v[68:69], s[2:3], v68, s76, v[142:143]
	s_mov_b64 s[12:13], 0xe00
	s_add_i32 s10, s46, s10
	v_lshl_add_u64 v[68:69], v[68:69], 0, s[12:13]
	s_mov_b32 m0, s10
	s_mov_b64 s[14:15], 0xc00
	global_load_lds_dwordx4 v[68:69], off
	s_add_i32 m0, m0, 0x1000
	v_lshl_add_u64 v[68:69], v[68:69], 0, s[100:101]
	global_load_lds_dwordx4 v[68:69], off
	v_add_u32_e32 v68, v2, v188
	v_mad_i64_i32 v[68:69], s[2:3], v68, s76, v[144:145]
	v_lshl_add_u64 v[68:69], v[68:69], 0, s[14:15]
	s_add_i32 m0, s10, 0x4000
	v_add_u32_e32 v2, v2, v168
	global_load_lds_dwordx4 v[68:69], off
	s_add_i32 m0, m0, 0x1000
	v_lshl_add_u64 v[68:69], v[68:69], 0, s[100:101]
	global_load_lds_dwordx4 v[68:69], off
	v_add_u32_e32 v68, v70, v169
	v_mad_i64_i32 v[68:69], s[2:3], v68, s76, v[142:143]
	v_lshl_add_u64 v[68:69], v[68:69], 0, s[12:13]
	s_add_i32 m0, s10, 0x2000
	s_nop 0
	global_load_lds_dwordx4 v[68:69], off
	s_add_i32 m0, m0, 0x1000
	v_lshl_add_u64 v[68:69], v[68:69], 0, s[100:101]
	global_load_lds_dwordx4 v[68:69], off
	v_mad_i64_i32 v[68:69], s[2:3], v2, s76, v[146:147]
	v_lshl_add_u64 v[68:69], v[68:69], 0, s[14:15]
	s_add_i32 m0, s10, 0x6000
	s_nop 0
	global_load_lds_dwordx4 v[68:69], off
	s_add_i32 m0, m0, 0x1000
	v_lshl_add_u64 v[68:69], v[68:69], 0, s[100:101]
	global_load_lds_dwordx4 v[68:69], off

	.amdhsa_kernel _Z6mk_fwd4Args
		.amdhsa_group_segment_fixed_size 0
		.amdhsa_private_segment_fixed_size 0
		.amdhsa_kernarg_size 504
		.amdhsa_user_sgpr_count 2
		.amdhsa_user_sgpr_dispatch_ptr 0
		.amdhsa_user_sgpr_queue_ptr 0
		.amdhsa_user_sgpr_kernarg_segment_ptr 1
		.amdhsa_user_sgpr_dispatch_id 0
		.amdhsa_user_sgpr_kernarg_preload_length 0
		.amdhsa_user_sgpr_kernarg_preload_offset 0
		.amdhsa_user_sgpr_private_segment_size 0
		.amdhsa_uses_dynamic_stack 0
		.amdhsa_enable_private_segment 0
		.amdhsa_system_sgpr_workgroup_id_x 1
		.amdhsa_system_sgpr_workgroup_id_y 0
		.amdhsa_system_sgpr_workgroup_id_z 0
		.amdhsa_system_sgpr_workgroup_info 0
		.amdhsa_system_vgpr_workitem_id 0
		.amdhsa_next_free_vgpr 256
		.amdhsa_next_free_sgpr 102
		.amdhsa_accum_offset 256
		.amdhsa_reserve_vcc 1
		.amdhsa_float_round_mode_32 0
		.amdhsa_float_round_mode_16_64 0
		.amdhsa_float_denorm_mode_32 3
		.amdhsa_float_denorm_mode_16_64 3
		.amdhsa_dx10_clamp 1
		.amdhsa_ieee_mode 1
		.amdhsa_fp16_overflow 0
		.amdhsa_tg_split 0
		.amdhsa_exception_fp_ieee_invalid_op 0
		.amdhsa_exception_fp_denorm_src 0
		.amdhsa_exception_fp_ieee_div_zero 0
		.amdhsa_exception_fp_ieee_overflow 0
		.amdhsa_exception_fp_ieee_underflow 0
		.amdhsa_exception_fp_ieee_inexact 0
		.amdhsa_exception_int_div_zero 0
	.end_amdhsa_kernel

amdhsa.kernels:
  - .agpr_count:     0
    .args:
      - .offset:         0
        .size:           248
        .value_kind:     by_value
      - .offset:         248
        .size:           4
        .value_kind:     hidden_block_count_x
      - .offset:         252
        .size:           4
        .value_kind:     hidden_block_count_y
      - .offset:         256
        .size:           4
        .value_kind:     hidden_block_count_z
      - .offset:         260
        .size:           2
        .value_kind:     hidden_group_size_x
      - .offset:         262
        .size:           2
        .value_kind:     hidden_group_size_y
      - .offset:         264
        .size:           2
        .value_kind:     hidden_group_size_z
      - .offset:         266
        .size:           2
        .value_kind:     hidden_remainder_x
      - .offset:         268
        .size:           2
        .value_kind:     hidden_remainder_y
      - .offset:         270
        .size:           2
        .value_kind:     hidden_remainder_z
      - .offset:         288
        .size:           8
        .value_kind:     hidden_global_offset_x
      - .offset:         296
        .size:           8
        .value_kind:     hidden_global_offset_y
      - .offset:         304
        .size:           8
        .value_kind:     hidden_global_offset_z
      - .offset:         312
        .size:           2
        .value_kind:     hidden_grid_dims
      - .offset:         368
        .size:           4
        .value_kind:     hidden_dynamic_lds_size
    .group_segment_fixed_size: 0
    .kernarg_segment_align: 8
    .kernarg_segment_size: 504
    .language:       OpenCL C
    .language_version:
      - 2
      - 0
    .max_flat_workgroup_size: 512
    .name:           _Z6mk_fwd4Args
    .private_segment_fixed_size: 0
    .sgpr_count:     108
    .sgpr_spill_count: 111
    .symbol:         _Z6mk_fwd4Args.kd
    .uniform_work_group_size: 1
    .uses_dynamic_stack: false
    .vgpr_count:     256
    .vgpr_spill_count: 0
    .wavefront_size: 64
